# GEMM unit accumulator zeroing: 128 v_mov_b32 -> 64 v_mov_b64 in 5 GEMM instantiations, on top of v23
# speedup vs baseline: 1.0046x; 1.0046x over previous
;     ...
; #pragma unroll
;         for (int a = 0; a < 2; ++a)
; #pragma unroll
;             for (int b = 0; b < 2; ++b)
; #pragma unroll
;                 for (int m = 0; m < 4; ++m)
; #pragma unroll
;                     for (int n = 0; n < 2; ++n) acc[a][b][m][n] = (f32x4){0.f, 0.f, 0.f, 0.f};
;         cur = nxt; cA = nA; cB = nB; ++ui; tbi = tbn;
.LBB0_235:
	s_lshl_b32 s48, s47, 19
	s_and_b64 s[56:57], s[0:1], exec
	s_cselect_b32 s52, s48, s54
	s_lshl_b32 s49, s46, 19
	s_and_b64 s[0:1], s[0:1], exec
	v_mov_b32_e32 v10, 0
	s_cselect_b32 s0, s49, s53
	s_add_i32 s1, s54, 0x40080
	s_addk_i32 s53, 0x100
	s_mov_b32 s54, -2
	v_mov_b64_e32 v[2:3], 0
	v_mov_b64_e32 v[4:5], 0
	v_mov_b64_e32 v[6:7], 0
	v_mov_b64_e32 v[8:9], 0
	v_mov_b32_e32 v11, 0
	v_mov_b64_e32 v[12:13], 0
	v_mov_b64_e32 v[14:15], 0
	v_mov_b64_e32 v[16:17], 0
	v_mov_b64_e32 v[18:19], 0
	v_mov_b64_e32 v[20:21], 0
	v_mov_b64_e32 v[22:23], 0
	v_mov_b64_e32 v[24:25], 0
	v_mov_b64_e32 v[26:27], 0
	v_mov_b64_e32 v[28:29], 0
	v_mov_b64_e32 v[30:31], 0
	v_mov_b64_e32 v[32:33], 0
	v_mov_b64_e32 v[34:35], 0
	v_mov_b64_e32 v[36:37], 0
	v_mov_b64_e32 v[38:39], 0
	v_mov_b64_e32 v[40:41], 0
	v_mov_b64_e32 v[42:43], 0
	v_mov_b64_e32 v[44:45], 0
	v_mov_b64_e32 v[46:47], 0
	v_mov_b64_e32 v[48:49], 0
	v_mov_b64_e32 v[50:51], 0
	v_mov_b64_e32 v[52:53], 0
	v_mov_b64_e32 v[54:55], 0
	v_mov_b64_e32 v[56:57], 0
	v_mov_b64_e32 v[58:59], 0
	v_mov_b64_e32 v[60:61], 0
	v_mov_b64_e32 v[62:63], 0
	v_mov_b64_e32 v[64:65], 0
	v_mov_b64_e32 v[66:67], 0
	v_mov_b64_e32 v[68:69], 0
	v_mov_b64_e32 v[70:71], 0
	v_mov_b64_e32 v[72:73], 0
	v_mov_b64_e32 v[74:75], 0
	v_mov_b64_e32 v[76:77], 0
	v_mov_b64_e32 v[78:79], 0
	v_mov_b64_e32 v[80:81], 0
	v_mov_b64_e32 v[82:83], 0
	v_mov_b64_e32 v[84:85], 0
	v_mov_b64_e32 v[86:87], 0
	v_mov_b64_e32 v[88:89], 0
	v_mov_b64_e32 v[90:91], 0
	v_mov_b64_e32 v[92:93], 0
	v_mov_b64_e32 v[94:95], 0
	v_mov_b64_e32 v[96:97], 0
	v_mov_b64_e32 v[98:99], 0
	v_mov_b64_e32 v[100:101], 0
	v_mov_b64_e32 v[102:103], 0
	v_mov_b64_e32 v[104:105], 0
	v_mov_b64_e32 v[106:107], 0
	v_mov_b64_e32 v[108:109], 0
	v_mov_b64_e32 v[110:111], 0
	v_mov_b64_e32 v[112:113], 0
	v_mov_b64_e32 v[114:115], 0
	v_mov_b64_e32 v[116:117], 0
	v_mov_b64_e32 v[118:119], 0
	v_mov_b64_e32 v[120:121], 0
	v_mov_b64_e32 v[122:123], 0
	v_mov_b64_e32 v[124:125], 0
	v_mov_b64_e32 v[126:127], 0
	v_mov_b64_e32 v[128:129], 0

;     ...
; #pragma unroll
;         for (int a = 0; a < 2; ++a)
; #pragma unroll
;             for (int b = 0; b < 2; ++b)
; #pragma unroll
;                 for (int m = 0; m < 4; ++m)
; #pragma unroll
;                     for (int n = 0; n < 2; ++n) acc[a][b][m][n] = (f32x4){0.f, 0.f, 0.f, 0.f};
;         cur = nxt; cA = nA; cB = nB; ++ui; tbi = tbn;
.LBB0_251:
	s_lshl_b32 s45, s17, 20
	s_and_b64 s[52:53], s[0:1], exec
	s_cselect_b32 s49, s45, s51
	s_lshl_b32 s46, s16, 20
	s_and_b64 s[0:1], s[0:1], exec
	v_mov_b32_e32 v10, 0
	s_cselect_b32 s0, s46, s50
	s_add_i32 s1, s51, 0x80080
	s_addk_i32 s50, 0x100
	s_mov_b32 s51, -2
	v_mov_b64_e32 v[2:3], 0
	v_mov_b64_e32 v[4:5], 0
	v_mov_b64_e32 v[6:7], 0
	v_mov_b64_e32 v[8:9], 0
	v_mov_b32_e32 v11, 0
	v_mov_b64_e32 v[12:13], 0
	v_mov_b64_e32 v[14:15], 0
	v_mov_b64_e32 v[16:17], 0
	v_mov_b64_e32 v[18:19], 0
	v_mov_b64_e32 v[20:21], 0
	v_mov_b64_e32 v[22:23], 0
	v_mov_b64_e32 v[24:25], 0
	v_mov_b64_e32 v[26:27], 0
	v_mov_b64_e32 v[28:29], 0
	v_mov_b64_e32 v[30:31], 0
	v_mov_b64_e32 v[32:33], 0
	v_mov_b64_e32 v[34:35], 0
	v_mov_b64_e32 v[36:37], 0
	v_mov_b64_e32 v[38:39], 0
	v_mov_b64_e32 v[40:41], 0
	v_mov_b64_e32 v[42:43], 0
	v_mov_b64_e32 v[44:45], 0
	v_mov_b64_e32 v[46:47], 0
	v_mov_b64_e32 v[48:49], 0
	v_mov_b64_e32 v[50:51], 0
	v_mov_b64_e32 v[52:53], 0
	v_mov_b64_e32 v[54:55], 0
	v_mov_b64_e32 v[56:57], 0
	v_mov_b64_e32 v[58:59], 0
	v_mov_b64_e32 v[60:61], 0
	v_mov_b64_e32 v[62:63], 0
	v_mov_b64_e32 v[64:65], 0
	v_mov_b64_e32 v[66:67], 0
	v_mov_b64_e32 v[68:69], 0
	v_mov_b64_e32 v[70:71], 0
	v_mov_b64_e32 v[72:73], 0
	v_mov_b64_e32 v[74:75], 0
	v_mov_b64_e32 v[76:77], 0
	v_mov_b64_e32 v[78:79], 0
	v_mov_b64_e32 v[80:81], 0
	v_mov_b64_e32 v[82:83], 0
	v_mov_b64_e32 v[84:85], 0
	v_mov_b64_e32 v[86:87], 0
	v_mov_b64_e32 v[88:89], 0
	v_mov_b64_e32 v[90:91], 0
	v_mov_b64_e32 v[92:93], 0
	v_mov_b64_e32 v[94:95], 0
	v_mov_b64_e32 v[96:97], 0
	v_mov_b64_e32 v[98:99], 0
	v_mov_b64_e32 v[100:101], 0
	v_mov_b64_e32 v[102:103], 0
	v_mov_b64_e32 v[104:105], 0
	v_mov_b64_e32 v[106:107], 0
	v_mov_b64_e32 v[108:109], 0
	v_mov_b64_e32 v[110:111], 0
	v_mov_b64_e32 v[112:113], 0
	v_mov_b64_e32 v[114:115], 0
	v_mov_b64_e32 v[116:117], 0
	v_mov_b64_e32 v[118:119], 0
	v_mov_b64_e32 v[120:121], 0
	v_mov_b64_e32 v[122:123], 0
	v_mov_b64_e32 v[124:125], 0
	v_mov_b64_e32 v[126:127], 0
	v_mov_b64_e32 v[128:129], 0

;     ...
; #pragma unroll
;         for (int a = 0; a < 2; ++a)
; #pragma unroll
;             for (int b = 0; b < 2; ++b)
; #pragma unroll
;                 for (int m = 0; m < 4; ++m)
; #pragma unroll
;                     for (int n = 0; n < 2; ++n) acc[a][b][m][n] = (f32x4){0.f, 0.f, 0.f, 0.f};
;         cur = nxt; cA = nA; cB = nB; ++ui; tbi = tbn;
.LBB0_263:
	s_lshl_b32 s58, s57, 19
	s_and_b64 s[14:15], s[0:1], exec
	s_cselect_b32 s62, s58, s64
	s_lshl_b32 s59, s56, 19
	s_and_b64 s[0:1], s[0:1], exec
	v_mov_b32_e32 v10, 0
	s_cselect_b32 s0, s59, s63
	s_add_i32 s1, s64, 0x40080
	s_addk_i32 s63, 0x100
	s_mov_b32 s64, -2
	v_mov_b64_e32 v[2:3], 0
	v_mov_b64_e32 v[4:5], 0
	v_mov_b64_e32 v[6:7], 0
	v_mov_b64_e32 v[8:9], 0
	v_mov_b32_e32 v11, 0
	v_mov_b64_e32 v[12:13], 0
	v_mov_b64_e32 v[14:15], 0
	v_mov_b64_e32 v[16:17], 0
	v_mov_b64_e32 v[18:19], 0
	v_mov_b64_e32 v[20:21], 0
	v_mov_b64_e32 v[22:23], 0
	v_mov_b64_e32 v[24:25], 0
	v_mov_b64_e32 v[26:27], 0
	v_mov_b64_e32 v[28:29], 0
	v_mov_b64_e32 v[30:31], 0
	v_mov_b64_e32 v[32:33], 0
	v_mov_b64_e32 v[34:35], 0
	v_mov_b64_e32 v[36:37], 0
	v_mov_b64_e32 v[38:39], 0
	v_mov_b64_e32 v[40:41], 0
	v_mov_b64_e32 v[42:43], 0
	v_mov_b64_e32 v[44:45], 0
	v_mov_b64_e32 v[46:47], 0
	v_mov_b64_e32 v[48:49], 0
	v_mov_b64_e32 v[50:51], 0
	v_mov_b64_e32 v[52:53], 0
	v_mov_b64_e32 v[54:55], 0
	v_mov_b64_e32 v[56:57], 0
	v_mov_b64_e32 v[58:59], 0
	v_mov_b64_e32 v[60:61], 0
	v_mov_b64_e32 v[62:63], 0
	v_mov_b64_e32 v[64:65], 0
	v_mov_b64_e32 v[66:67], 0
	v_mov_b64_e32 v[68:69], 0
	v_mov_b64_e32 v[70:71], 0
	v_mov_b64_e32 v[72:73], 0
	v_mov_b64_e32 v[74:75], 0
	v_mov_b64_e32 v[76:77], 0
	v_mov_b64_e32 v[78:79], 0
	v_mov_b64_e32 v[80:81], 0
	v_mov_b64_e32 v[82:83], 0
	v_mov_b64_e32 v[84:85], 0
	v_mov_b64_e32 v[86:87], 0
	v_mov_b64_e32 v[88:89], 0
	v_mov_b64_e32 v[90:91], 0
	v_mov_b64_e32 v[92:93], 0
	v_mov_b64_e32 v[94:95], 0
	v_mov_b64_e32 v[96:97], 0
	v_mov_b64_e32 v[98:99], 0
	v_mov_b64_e32 v[100:101], 0
	v_mov_b64_e32 v[102:103], 0
	v_mov_b64_e32 v[104:105], 0
	v_mov_b64_e32 v[106:107], 0
	v_mov_b64_e32 v[108:109], 0
	v_mov_b64_e32 v[110:111], 0
	v_mov_b64_e32 v[112:113], 0
	v_mov_b64_e32 v[114:115], 0
	v_mov_b64_e32 v[116:117], 0
	v_mov_b64_e32 v[118:119], 0
	v_mov_b64_e32 v[120:121], 0
	v_mov_b64_e32 v[122:123], 0
	v_mov_b64_e32 v[124:125], 0
	v_mov_b64_e32 v[126:127], 0
	v_mov_b64_e32 v[128:129], 0

;     ...
; #pragma unroll
;         for (int a = 0; a < 2; ++a)
; #pragma unroll
;             for (int b = 0; b < 2; ++b)
; #pragma unroll
;                 for (int m = 0; m < 4; ++m)
; #pragma unroll
;                     for (int n = 0; n < 2; ++n) acc[a][b][m][n] = (f32x4){0.f, 0.f, 0.f, 0.f};
;         cur = nxt; cA = nA; cB = nB; ++ui; tbi = tbn;
.LBB0_990:
	s_lshl_b32 s0, s64, 19
	s_and_b64 s[22:23], s[34:35], exec
	s_cselect_b32 s1, s0, s68
	s_add_i32 s18, s18, 0
	s_add_i32 s18, s18, 0x20000
	v_mov_b32_e32 v34, 0
	v_add3_u32 v180, s18, v171, v172
	v_add3_u32 v181, s18, v173, v174
	s_mov_b32 s70, -2
	s_movk_i32 s71, 0x100
	v_mov_b64_e32 v[18:19], 0
	v_mov_b64_e32 v[20:21], 0
	v_mov_b64_e32 v[22:23], 0
	v_mov_b64_e32 v[24:25], 0
	v_mov_b64_e32 v[26:27], 0
	v_mov_b64_e32 v[28:29], 0
	v_mov_b64_e32 v[30:31], 0
	v_mov_b64_e32 v[32:33], 0
	v_mov_b32_e32 v35, 0
	v_mov_b64_e32 v[36:37], 0
	v_mov_b64_e32 v[38:39], 0
	v_mov_b64_e32 v[40:41], 0
	v_mov_b64_e32 v[42:43], 0
	v_mov_b64_e32 v[44:45], 0
	v_mov_b64_e32 v[46:47], 0
	v_mov_b64_e32 v[48:49], 0
	v_mov_b64_e32 v[50:51], 0
	v_mov_b64_e32 v[52:53], 0
	v_mov_b64_e32 v[54:55], 0
	v_mov_b64_e32 v[56:57], 0
	v_mov_b64_e32 v[58:59], 0
	v_mov_b64_e32 v[60:61], 0
	v_mov_b64_e32 v[62:63], 0
	v_mov_b64_e32 v[64:65], 0
	v_mov_b64_e32 v[66:67], 0
	v_mov_b64_e32 v[68:69], 0
	v_mov_b64_e32 v[70:71], 0
	v_mov_b64_e32 v[72:73], 0
	v_mov_b64_e32 v[74:75], 0
	v_mov_b64_e32 v[76:77], 0
	v_mov_b64_e32 v[78:79], 0
	v_mov_b64_e32 v[80:81], 0
	v_mov_b64_e32 v[82:83], 0
	v_mov_b64_e32 v[84:85], 0
	v_mov_b64_e32 v[86:87], 0
	v_mov_b64_e32 v[88:89], 0
	v_mov_b64_e32 v[90:91], 0
	v_mov_b64_e32 v[92:93], 0
	v_mov_b64_e32 v[94:95], 0
	v_mov_b64_e32 v[96:97], 0
	v_mov_b64_e32 v[98:99], 0
	v_mov_b64_e32 v[100:101], 0
	v_mov_b64_e32 v[102:103], 0
	v_mov_b64_e32 v[104:105], 0
	v_mov_b64_e32 v[106:107], 0
	v_mov_b64_e32 v[108:109], 0
	v_mov_b64_e32 v[110:111], 0
	v_mov_b64_e32 v[112:113], 0
	v_mov_b64_e32 v[114:115], 0
	v_mov_b64_e32 v[116:117], 0
	v_mov_b64_e32 v[118:119], 0
	v_mov_b64_e32 v[120:121], 0
	v_mov_b64_e32 v[122:123], 0
	v_mov_b64_e32 v[124:125], 0
	v_mov_b64_e32 v[126:127], 0
	v_mov_b64_e32 v[128:129], 0
	v_mov_b64_e32 v[130:131], 0
	v_mov_b64_e32 v[132:133], 0
	v_mov_b64_e32 v[134:135], 0
	v_mov_b64_e32 v[136:137], 0
	v_mov_b64_e32 v[138:139], 0
	v_mov_b64_e32 v[140:141], 0
	v_mov_b64_e32 v[142:143], 0
	v_mov_b64_e32 v[144:145], 0
	s_branch .LBB0_992

;     ...
; #pragma unroll
;         for (int a = 0; a < 2; ++a)
; #pragma unroll
;             for (int b = 0; b < 2; ++b)
; #pragma unroll
;                 for (int m = 0; m < 4; ++m)
; #pragma unroll
;                     for (int n = 0; n < 2; ++n) acc[a][b][m][n] = (f32x4){0.f, 0.f, 0.f, 0.f};
;         cur = nxt; cA = nA; cB = nB; ++ui; tbi = tbn;
.LBB0_1080:
	s_lshl_b32 s10, s60, 19
	s_and_b64 s[18:19], s[0:1], exec
	s_cselect_b32 s18, s10, s67
	s_lshl_b32 s11, s62, 19
	s_and_b64 s[0:1], s[0:1], exec
	v_mov_b32_e32 v26, 0
	s_cselect_b32 s0, s11, s66
	s_add_i32 s1, s67, 0x40080
	s_add_i32 s19, s66, 0x100
	s_mov_b32 s66, -2
	v_mov_b64_e32 v[2:3], 0
	v_mov_b64_e32 v[4:5], 0
	v_mov_b64_e32 v[6:7], 0
	v_mov_b64_e32 v[8:9], 0
	v_mov_b64_e32 v[10:11], 0
	v_mov_b64_e32 v[12:13], 0
	v_mov_b64_e32 v[14:15], 0
	v_mov_b64_e32 v[16:17], 0
	v_mov_b64_e32 v[18:19], 0
	v_mov_b64_e32 v[20:21], 0
	v_mov_b64_e32 v[22:23], 0
	v_mov_b64_e32 v[24:25], 0
	v_mov_b32_e32 v27, 0
	v_mov_b64_e32 v[28:29], 0
	v_mov_b64_e32 v[30:31], 0
	v_mov_b64_e32 v[32:33], 0
	v_mov_b64_e32 v[34:35], 0
	v_mov_b64_e32 v[36:37], 0
	v_mov_b64_e32 v[38:39], 0
	v_mov_b64_e32 v[40:41], 0
	v_mov_b64_e32 v[42:43], 0
	v_mov_b64_e32 v[44:45], 0
	v_mov_b64_e32 v[46:47], 0
	v_mov_b64_e32 v[48:49], 0
	v_mov_b64_e32 v[50:51], 0
	v_mov_b64_e32 v[52:53], 0
	v_mov_b64_e32 v[54:55], 0
	v_mov_b64_e32 v[56:57], 0
	v_mov_b64_e32 v[58:59], 0
	v_mov_b64_e32 v[60:61], 0
	v_mov_b64_e32 v[62:63], 0
	v_mov_b64_e32 v[64:65], 0
	v_mov_b64_e32 v[66:67], 0
	v_mov_b64_e32 v[68:69], 0
	v_mov_b64_e32 v[70:71], 0
	v_mov_b64_e32 v[72:73], 0
	v_mov_b64_e32 v[74:75], 0
	v_mov_b64_e32 v[76:77], 0
	v_mov_b64_e32 v[78:79], 0
	v_mov_b64_e32 v[80:81], 0
	v_mov_b64_e32 v[82:83], 0
	v_mov_b64_e32 v[84:85], 0
	v_mov_b64_e32 v[86:87], 0
	v_mov_b64_e32 v[88:89], 0
	v_mov_b64_e32 v[90:91], 0
	v_mov_b64_e32 v[92:93], 0
	v_mov_b64_e32 v[94:95], 0
	v_mov_b64_e32 v[96:97], 0
	v_mov_b64_e32 v[98:99], 0
	v_mov_b64_e32 v[100:101], 0
	v_mov_b64_e32 v[102:103], 0
	v_mov_b64_e32 v[104:105], 0
	v_mov_b64_e32 v[106:107], 0
	v_mov_b64_e32 v[108:109], 0
	v_mov_b64_e32 v[110:111], 0
	v_mov_b64_e32 v[112:113], 0
	v_mov_b64_e32 v[114:115], 0
	v_mov_b64_e32 v[116:117], 0
	v_mov_b64_e32 v[118:119], 0
	v_mov_b64_e32 v[120:121], 0
	v_mov_b64_e32 v[122:123], 0
	v_mov_b64_e32 v[124:125], 0
	v_mov_b64_e32 v[134:135], 0
	v_mov_b64_e32 v[136:137], 0
